# deferred weight-conversion split 3400 + 1700, idle-slot quotas 6/9/7/11
# baseline (speedup 1.0000x reference)
; #define LAS __attribute__((address_space(3)))
; #define SEAM(k) do { if (IN(k) && IN((k) + 1)) xcd_barrier(bar); \
;         if (PROBE_MASK) { const unsigned long long t_ = __builtin_amdgcn_s_memrealtime(); if ((PROBE_MASK >> (k)) & 1u) pr_acc += t_ - pr_t0; pr_t0 = t_; } } while (0)
; __device__ __forceinline__ void convert_deferred(const Ptrs& P, unsigned char* lds, int quota) {
;     const int tid = threadIdx.x, wid = tid >> 6, lane = tid & 63;
;     float* tile = (float*)lds;
;     volatile __attribute__((address_space(3))) int* slot = (volatile __attribute__((address_space(3))) int*)((__attribute__((address_space(3))) unsigned char*)lds + 131072 + 320 + 11000);
;     unsigned* q = (unsigned*)(P.ws + WS_CTL) + CW_DEFQ;
;     for (int n = 0; n < quota; ++n) {
;         __syncthreads();
;         if (tid == 0) *slot = (int)atomicAdd(q, 1u);
;         __syncthreads();
;         const int t = *slot;
;         if (t >= DEF_GU + DEF_DN) break;
;         const bool gu = t < DEF_GU;
;         const float* src = gu ? P.in[34] : P.in[36]; bf16* dst = (bf16*)(P.ws + (gu ? WS_WGU : WS_WDN));
;         const int N = gu ? 2048 : 1024, ntn = N / 256, it = gu ? 2 * NE * 16 * 8 - DEF_GU + t : 2 * NE * 16 * 4 - DEF_DN + (t - DEF_GU);
; __global__ void __launch_bounds__(NT, 2) mega(Args args) {
;     ...
;         { const int rem_ = ((LAS int*)(LDSP + MISC_OFF + 256))[96] % G; if (rem_ != 0 && vcu >= rem_) convert_deferred(P, lds, 5); } } SEAM(9);
.LBB0_1609:
	s_abs_i32 s0, s62
	v_cvt_f32_u32_e32 v2, s0
	s_sub_i32 s5, 0, s0
	s_abs_i32 s4, s9
	s_ashr_i32 s3, s9, 31
	v_rcp_iflag_f32_e32 v2, v2
	s_mov_b32 s1, 0
	v_mul_f32_e32 v2, 0x4f7ffffe, v2
	v_cvt_u32_f32_e32 v2, v2
	s_nop 0
	v_readfirstlane_b32 s6, v2
	s_mul_i32 s5, s5, s6
	s_mul_hi_u32 s5, s6, s5
	s_add_i32 s6, s6, s5
	s_mul_hi_u32 s5, s4, s6
	s_mul_i32 s5, s5, s0
	s_sub_i32 s4, s4, s5
	s_sub_i32 s5, s4, s0
	s_cmp_ge_u32 s4, s0
	s_cselect_b32 s4, s5, s4
	s_sub_i32 s5, s4, s0
	s_cmp_ge_u32 s4, s0
	s_cselect_b32 s0, s5, s4
	s_xor_b32 s0, s0, s3
	s_sub_i32 s0, s0, s3
	s_cmp_eq_u32 s0, 0
	v_readlane_b32 s3, v254, 2
	s_cselect_b64 s[4:5], -1, 0
	s_cmp_lt_i32 s3, s0
	s_cselect_b64 s[6:7], -1, 0
	s_or_b64 s[4:5], s[4:5], s[6:7]
	s_and_b64 vcc, exec, s[4:5]
	s_cbranch_vccnz .LBB0_1619
	v_and_b32_e32 v2, 0x7c, v175
	v_lshlrev_b32_e32 v3, 5, v0
	s_movk_i32 s0, 0x400
	v_and_or_b32 v12, v3, s0, v2
	v_bfe_u32 v2, v0, 3, 3
	v_lshl_or_b32 v4, v1, 5, v2
	v_lshlrev_b32_e32 v2, 3, v0
	v_lshl_add_u32 v11, v182, 4, 0
	v_and_b32_e32 v2, 56, v2
	v_mul_u32_u24_e32 v16, 0x2020, v1
	v_mov_b32_e32 v3, 0
	v_lshl_add_u32 v27, v4, 2, 0
	v_mul_u32_u24_e32 v28, 0x404, v2
	v_lshlrev_b32_e32 v10, 6, v4
	s_add_i32 s10, 0, 0x22c38
	v_add_u32_e32 v16, v11, v16
	s_mov_b32 s3, 7
	v_and_b32_e32 v13, 0xfc, v175
	v_and_b32_e32 v14, 56, v173
	v_or_b32_e32 v4, 0x200, v10
	v_mov_b32_e32 v5, v3
	v_or_b32_e32 v6, 0x400, v10
	v_mov_b32_e32 v7, v3
	v_or_b32_e32 v8, 0x600, v10
	v_mov_b32_e32 v9, v3
	v_mov_b32_e32 v15, s10
	s_movk_i32 s11, 0x13eb
	s_movk_i32 s12, 0x800
	s_mov_b32 s13, 0x1104e000
	s_movk_i32 s14, -1004
	v_add_u32_e32 v17, 0x404, v16
	v_add_u32_e32 v18, 0x40c, v16
	v_add_u32_e32 v19, 0x808, v16
	v_add_u32_e32 v20, 0xc0c, v16
	v_add_u32_e32 v21, 0xc14, v16
	v_add_u32_e32 v22, 0x1414, v16
	v_add_u32_e32 v23, 0x141c, v16
	v_add_u32_e32 v24, 0x1818, v16
	v_add_u32_e32 v25, 0x1c1c, v16
	v_add_u32_e32 v26, 0x1c24, v16
	v_lshlrev_b32_e32 v2, 1, v2
	v_add_u32_e32 v27, v27, v28
	v_lshlrev_b32_e32 v10, 1, v10
	s_branch .LBB0_1612

; #define SEAM(k) do { if (IN(k) && IN((k) + 1)) xcd_barrier(bar); \
;         if (PROBE_MASK) { const unsigned long long t_ = __builtin_amdgcn_s_memrealtime(); if ((PROBE_MASK >> (k)) & 1u) pr_acc += t_ - pr_t0; pr_t0 = t_; } } while (0)
; __device__ __forceinline__ void convert_deferred(const Ptrs& P, unsigned char* lds, int quota) {
;     const int tid = threadIdx.x, wid = tid >> 6, lane = tid & 63;
;     float* tile = (float*)lds;
;     volatile __attribute__((address_space(3))) int* slot = (volatile __attribute__((address_space(3))) int*)((__attribute__((address_space(3))) unsigned char*)lds + 131072 + 320 + 11000);
;     unsigned* q = (unsigned*)(P.ws + WS_CTL) + CW_DEFQ;
;     for (int n = 0; n < quota; ++n) {
;         __syncthreads();
;         if (tid == 0) *slot = (int)atomicAdd(q, 1u);
;         __syncthreads();
;         const int t = *slot;
;         if (t >= DEF_GU + DEF_DN) break;
;         const bool gu = t < DEF_GU;
;         const float* src = gu ? P.in[34] : P.in[36]; bf16* dst = (bf16*)(P.ws + (gu ? WS_WGU : WS_WDN));
;         const int N = gu ? 2048 : 1024, ntn = N / 256, it = gu ? 2 * NE * 16 * 8 - DEF_GU + t : 2 * NE * 16 * 4 - DEF_DN + (t - DEF_GU);
; __global__ void __launch_bounds__(NT, 2) mega(Args args) {
;     ...
;         if (IDLE_LAST(68 * 12)) convert_deferred(P, lds, 4); } SEAM(11);
.LBB0_1851:
	s_abs_i32 s0, s62
	v_cvt_f32_u32_e32 v2, s0
	s_sub_i32 s3, 0, s0
	v_readlane_b32 s56, v254, 40
	s_mov_b32 s1, 0
	v_rcp_iflag_f32_e32 v2, v2
	v_readlane_b32 s57, v254, 41
	v_mul_f32_e32 v2, 0x4f7ffffe, v2
	v_cvt_u32_f32_e32 v2, v2
	s_nop 0
	v_readfirstlane_b32 s4, v2
	s_mul_i32 s3, s3, s4
	s_mul_hi_u32 s3, s4, s3
	s_add_i32 s4, s4, s3
	s_mul_hi_u32 s3, s4, 0x330
	s_mul_i32 s3, s3, s0
	s_sub_i32 s3, 0x330, s3
	s_sub_i32 s4, s3, s0
	s_cmp_ge_u32 s3, s0
	s_cselect_b32 s3, s4, s3
	s_sub_i32 s4, s3, s0
	s_cmp_ge_u32 s3, s0
	s_cselect_b32 s0, s4, s3
	s_cmp_eq_u32 s0, 0
	s_cselect_b64 s[4:5], -1, 0
	s_cmp_lt_i32 s2, s0
	s_cselect_b64 s[6:7], -1, 0
	s_or_b64 s[4:5], s[4:5], s[6:7]
	s_and_b64 vcc, exec, s[4:5]
	s_cbranch_vccnz .LBB0_1861
	v_and_b32_e32 v2, 0x7c, v218
	v_lshlrev_b32_e32 v3, 5, v0
	s_movk_i32 s0, 0x400
	v_and_or_b32 v12, v3, s0, v2
	v_bfe_u32 v2, v0, 3, 3
	v_lshl_or_b32 v4, v1, 5, v2
	v_lshlrev_b32_e32 v2, 3, v0
	v_lshl_add_u32 v11, v182, 4, 0
	v_and_b32_e32 v2, 56, v2
	v_mul_u32_u24_e32 v16, 0x2020, v1
	v_mov_b32_e32 v3, 0
	s_waitcnt vmcnt(0)
	v_lshl_add_u32 v27, v4, 2, 0
	v_mul_u32_u24_e32 v28, 0x404, v2
	v_lshlrev_b32_e32 v10, 6, v4
	s_add_i32 s10, 0, 0x22c38
	v_add_u32_e32 v16, v11, v16
	v_and_b32_e32 v13, 0xfc, v218
	v_and_b32_e32 v14, 56, v179
	s_mov_b32 s3, 11
	v_or_b32_e32 v4, 0x200, v10
	v_mov_b32_e32 v5, v3
	v_or_b32_e32 v6, 0x400, v10
	v_mov_b32_e32 v7, v3
	v_or_b32_e32 v8, 0x600, v10
	v_mov_b32_e32 v9, v3
	v_mov_b32_e32 v15, s10
	s_movk_i32 s11, 0x13eb
	s_movk_i32 s12, 0x800
	s_mov_b32 s13, 0x1104e000
	s_movk_i32 s14, -1004
	v_add_u32_e32 v17, 0x404, v16
	v_add_u32_e32 v18, 0x40c, v16
	v_add_u32_e32 v19, 0x808, v16
	v_add_u32_e32 v20, 0xc0c, v16
	v_add_u32_e32 v21, 0xc14, v16
	v_add_u32_e32 v22, 0x1414, v16
	v_add_u32_e32 v23, 0x141c, v16
	v_add_u32_e32 v24, 0x1818, v16
	v_add_u32_e32 v25, 0x1c1c, v16
	v_add_u32_e32 v26, 0x1c24, v16
	v_lshlrev_b32_e32 v2, 1, v2
	v_add_u32_e32 v27, v27, v28
	v_lshlrev_b32_e32 v10, 1, v10
	s_branch .LBB0_1854
